# v038
# speedup vs baseline: 1.1071x; 1.0008x over previous
.LBB4_20:
	s_or_b64 exec, exec, s[10:11]
	s_cmp_lg_u64 s[6:7], 0
	s_cbranch_scc1 .Lmy_dec_nowait
	s_waitcnt vmcnt(0)
.Lmy_dec_nowait:
	v_mov_b64_e32 v[20:21], v[2:3]
	v_mov_b64_e32 v[18:19], v[0:1]
